# dense layer-2 fp8 up-projection epilogue regenerated with packed f32 math too (on top of MoE epilogue + MLA loop changes)
# baseline (speedup 1.0000x reference)
; #define PG8_LAS __attribute__((address_space(3)))
; __device__ __forceinline__ u32x4 pack8(const f32x4 a, const f32x4 b) { u32x4 w; w.x = cvt_pk_bf16(a[0], a[1]); w.y = cvt_pk_bf16(a[2], a[3]); w.z = cvt_pk_bf16(b[0], b[1]); w.w = cvt_pk_bf16(b[2], b[3]); return w; }
; __device__ __forceinline__ float silu_f(float x) { return x * __builtin_amdgcn_rcpf(1.0f + __builtin_amdgcn_exp2f(-1.4426950409f * x)); }
; template <int NP4, int PITCH, int OFF>
; __device__ __forceinline__ void rs_table(const float* part, int rowbase, int wr, int lane, float inv_dim, PG8_LAS float* t) {
;     f32x4 s[2][NP4];
; #pragma unroll
;     for (int ai = 0; ai < 2; ++ai) { const f32x4* p = (const f32x4*)(part + (size_t)(rowbase + ai * 128 + wr * 64 + lane) * PITCH + OFF);
; #pragma unroll
;         for (int j = 0; j < NP4; ++j) s[ai][j] = p[j]; }
; #pragma unroll
;     for (int ai = 0; ai < 2; ++ai) { f32x4 a = s[ai][0];
; #pragma unroll
;         for (int j = 1; j < NP4; ++j) a += s[ai][j];
;         t[ai * 64 + lane] = __builtin_amdgcn_rsqf(((a[0] + a[1]) + (a[2] + a[3])) * inv_dim + 1e-6f); }
;     asm volatile("s_waitcnt lgkmcnt(0)" ::: "memory");
;     __device__ __forceinline__ void operator()(const f32x4 (&acc)[2][2][4][2], const Unit& u, int wr, int wc, int fr, int fq) const {
;     ...
;             PG8_LAS float* t = tab + wid * 128; rs_table<4, 16, 0>(part, u.pm * BM, wr, lane, 1.0f / DM, t);
; #pragma unroll
;             for (int ai = 0; ai < 2; ++ai)
; #pragma unroll
;                 for (int m = 0; m < 4; ++m) rs[ai][m] = t[ai * 64 + m * 16 + fr];
;         }
;         const int row0 = u.pm * BM + wr * 64 + fr, col0 = u.pn * HALF + wc * 32 + 8 * fq;
; #pragma unroll
;         for (int ai = 0; ai < 2; ++ai)
; #pragma unroll
;             for (int m = 0; m < 4; ++m) {
;                 const float r = rs[ai][m]; f32x4 o[2];
; #pragma unroll
;                 for (int n = 0; n < 2; ++n) { const f32x4 a = acc[ai][0][m][n] * r, b = acc[ai][1][m][n] * r;
;                     o[n] = (f32x4){silu_f(a[0]) * b[0], silu_f(a[1]) * b[1], silu_f(a[2]) * b[2], silu_f(a[3]) * b[3]}; }
;                 if (F8OUT) { u32x2 w; w.x = pack4_fp8(o[0]); w.y = pack4_fp8(o[1]); *(u32x2*)((unsigned char*)h + (size_t)(row0 + ai * HALF + m * 16) * FFN + col0) = w; }
;                 else *(u32x4*)(h + (size_t)(row0 + ai * HALF + m * 16) * FFN + col0) = pack8(o[0], o[1]);
.LBB0_1731:
	s_lshl_b32 s24, s57, 8
	s_add_i32 s24, s24, s50
	v_or_b32_e32 v18, s24, v188
	v_ashrrev_i32_e32 v19, 31, v18
	v_lshlrev_b64 v[2:3], 6, v[18:19]
	s_nop 15
	s_nop 15
	v_lshl_add_u64 v[14:15], s[20:21], 0, v[2:3]
	global_load_dwordx4 v[2:5], v[14:15], off offset:48
	global_load_dwordx4 v[6:9], v[14:15], off offset:32
	global_load_dwordx4 v[10:13], v[14:15], off
	s_nop 0
	global_load_dwordx4 v[14:17], v[14:15], off offset:16
	v_add_u32_e32 v18, 0x80, v18
	v_ashrrev_i32_e32 v19, 31, v18
	v_lshlrev_b64 v[18:19], 6, v[18:19]
	v_lshl_add_u64 v[30:31], s[20:21], 0, v[18:19]
	global_load_dwordx4 v[18:21], v[30:31], off offset:48
	global_load_dwordx4 v[22:25], v[30:31], off offset:32
	global_load_dwordx4 v[26:29], v[30:31], off
	s_nop 0
	global_load_dwordx4 v[30:33], v[30:31], off offset:16
	s_and_b64 vcc, exec, s[2:3]
	s_waitcnt vmcnt(0)
	v_pk_add_f32 v[12:13], v[12:13], v[16:17]
	v_pk_add_f32 v[10:11], v[10:11], v[14:15]
	v_pk_add_f32 v[8:9], v[12:13], v[8:9]
	v_pk_add_f32 v[6:7], v[10:11], v[6:7]
	v_pk_add_f32 v[4:5], v[8:9], v[4:5]
	v_pk_add_f32 v[2:3], v[6:7], v[2:3]
	v_or_b32_e32 v14, s24, v163
	v_add_f32_e32 v2, v2, v3
	v_add_f32_e32 v3, v4, v5
	v_add_f32_e32 v2, v2, v3
	v_fmamk_f32 v2, v2, 0x3a800000, v248
	v_rsq_f32_e32 v6, v2
	v_pk_add_f32 v[2:3], v[28:29], v[32:33]
	v_pk_add_f32 v[4:5], v[26:27], v[30:31]
	v_pk_add_f32 v[2:3], v[2:3], v[24:25]
	v_pk_add_f32 v[4:5], v[4:5], v[22:23]
	v_pk_add_f32 v[2:3], v[2:3], v[20:21]
	v_pk_add_f32 v[4:5], v[4:5], v[18:19]
	v_add_f32_e32 v2, v2, v3
	v_add_f32_e32 v4, v4, v5
	v_add_f32_e32 v2, v4, v2
	v_fmamk_f32 v2, v2, 0x3a800000, v248
	v_rsq_f32_e32 v2, v2
	ds_write2st64_b32 v189, v6, v2 offset1:1
	s_waitcnt lgkmcnt(0)
	ds_read2_b32 v[10:11], v190 offset1:16
	ds_read2_b32 v[8:9], v190 offset0:32 offset1:48
	ds_read2_b32 v[6:7], v190 offset0:64 offset1:80
	ds_read2_b32 v[4:5], v190 offset0:96 offset1:112
	v_lshl_or_b32 v2, s56, 7, v187
	s_waitcnt lgkmcnt(0)
	v_ashrrev_i32_e32 v3, 31, v2
	v_lshl_add_u64 v[2:3], s[12:13], 0, v[2:3]
	v_mov_b32_e32 v33, 0xbfb8aa3b
	v_mov_b32_e32 v32, 0x41000000
	v_mov_b32_e32 v15, 1.0
	v_pk_mul_f32 v[16:17], v[154:155], v[10:11] op_sel_hi:[1,0]
	v_pk_mul_f32 v[18:19], v[156:157], v[10:11] op_sel_hi:[1,0]
	v_pk_mul_f32 v[20:21], v[150:151], v[10:11] op_sel_hi:[1,0]
	v_pk_mul_f32 v[22:23], v[152:153], v[10:11] op_sel_hi:[1,0]
	v_pk_mul_f32 v[24:25], v[16:17], v[32:33] op_sel:[0,1]
	v_pk_mul_f32 v[26:27], v[18:19], v[32:33] op_sel:[0,1]
	v_pk_mul_f32 v[28:29], v[20:21], v[32:33] op_sel:[0,1]
	v_pk_mul_f32 v[30:31], v[22:23], v[32:33] op_sel:[0,1]
	v_exp_f32_e32 v24, v24
	v_exp_f32_e32 v25, v25
	v_exp_f32_e32 v26, v26
	v_exp_f32_e32 v27, v27
	v_exp_f32_e32 v28, v28
	v_exp_f32_e32 v29, v29
	v_exp_f32_e32 v30, v30
	v_exp_f32_e32 v31, v31
	v_pk_add_f32 v[24:25], v[24:25], v[14:15] op_sel:[0,1]
	v_pk_add_f32 v[26:27], v[26:27], v[14:15] op_sel:[0,1]
	v_pk_add_f32 v[28:29], v[28:29], v[14:15] op_sel:[0,1]
	v_pk_add_f32 v[30:31], v[30:31], v[14:15] op_sel:[0,1]
	v_rcp_f32_e32 v24, v24
	v_rcp_f32_e32 v25, v25
	v_rcp_f32_e32 v26, v26
	v_rcp_f32_e32 v27, v27
	v_rcp_f32_e32 v28, v28
	v_rcp_f32_e32 v29, v29
	v_rcp_f32_e32 v30, v30
	v_rcp_f32_e32 v31, v31
	v_pk_mul_f32 v[24:25], v[16:17], v[24:25]
	v_pk_mul_f32 v[26:27], v[18:19], v[26:27]
	v_pk_mul_f32 v[28:29], v[20:21], v[28:29]
	v_pk_mul_f32 v[30:31], v[22:23], v[30:31]
	v_pk_mul_f32 v[16:17], v[158:159], v[10:11] op_sel_hi:[1,0]
	v_pk_mul_f32 v[18:19], v[160:161], v[10:11] op_sel_hi:[1,0]
	v_pk_mul_f32 v[20:21], v[146:147], v[10:11] op_sel_hi:[1,0]
	v_pk_mul_f32 v[22:23], v[148:149], v[10:11] op_sel_hi:[1,0]
	v_pk_mul_f32 v[24:25], v[16:17], v[24:25]
	v_pk_mul_f32 v[26:27], v[18:19], v[26:27]
	v_pk_mul_f32 v[28:29], v[20:21], v[28:29]
	v_pk_mul_f32 v[30:31], v[22:23], v[30:31]
	v_pk_mul_f32 v[24:25], v[24:25], v[32:33] op_sel_hi:[1,0]
	v_pk_mul_f32 v[26:27], v[26:27], v[32:33] op_sel_hi:[1,0]
	v_pk_mul_f32 v[28:29], v[28:29], v[32:33] op_sel_hi:[1,0]
	v_pk_mul_f32 v[30:31], v[30:31], v[32:33] op_sel_hi:[1,0]
	v_med3_f32 v24, v24, s64, v250
	v_med3_f32 v25, v25, s64, v250
	v_med3_f32 v26, v26, s64, v250
	v_med3_f32 v27, v27, s64, v250
	v_med3_f32 v28, v28, s64, v250
	v_med3_f32 v29, v29, s64, v250
	v_med3_f32 v30, v30, s64, v250
	v_med3_f32 v31, v31, s64, v250
	v_cvt_pk_fp8_f32 v12, v24, v25
	v_cvt_pk_fp8_f32 v13, v28, v29
	s_nop 0
	v_cvt_pk_fp8_f32 v12, v26, v27 op_sel:[0,0,1]
	v_cvt_pk_fp8_f32 v13, v30, v31 op_sel:[0,0,1]
	v_mad_i64_i32 v[16:17], s[24:25], v14, s73, v[2:3]
	global_store_dwordx2 v[16:17], v[12:13], off
	v_pk_mul_f32 v[16:17], v[142:143], v[10:11] op_sel:[0,1]
	v_pk_mul_f32 v[18:19], v[144:145], v[10:11] op_sel:[0,1]
	v_pk_mul_f32 v[20:21], v[134:135], v[10:11] op_sel:[0,1]
	v_pk_mul_f32 v[22:23], v[136:137], v[10:11] op_sel:[0,1]
	v_pk_mul_f32 v[24:25], v[16:17], v[32:33] op_sel:[0,1]
	v_pk_mul_f32 v[26:27], v[18:19], v[32:33] op_sel:[0,1]
	v_pk_mul_f32 v[28:29], v[20:21], v[32:33] op_sel:[0,1]
	v_pk_mul_f32 v[30:31], v[22:23], v[32:33] op_sel:[0,1]
	v_exp_f32_e32 v24, v24
	v_exp_f32_e32 v25, v25
	v_exp_f32_e32 v26, v26
	v_exp_f32_e32 v27, v27
	v_exp_f32_e32 v28, v28
	v_exp_f32_e32 v29, v29
	v_exp_f32_e32 v30, v30
	v_exp_f32_e32 v31, v31
	v_pk_add_f32 v[24:25], v[24:25], v[14:15] op_sel:[0,1]
	v_pk_add_f32 v[26:27], v[26:27], v[14:15] op_sel:[0,1]
	v_pk_add_f32 v[28:29], v[28:29], v[14:15] op_sel:[0,1]
	v_pk_add_f32 v[30:31], v[30:31], v[14:15] op_sel:[0,1]
	v_rcp_f32_e32 v24, v24
	v_rcp_f32_e32 v25, v25
	v_rcp_f32_e32 v26, v26
	v_rcp_f32_e32 v27, v27
	v_rcp_f32_e32 v28, v28
	v_rcp_f32_e32 v29, v29
	v_rcp_f32_e32 v30, v30
	v_rcp_f32_e32 v31, v31
	v_pk_mul_f32 v[24:25], v[16:17], v[24:25]
; #define PG8_LAS __attribute__((address_space(3)))
; __device__ __forceinline__ u32x4 pack8(const f32x4 a, const f32x4 b) { u32x4 w; w.x = cvt_pk_bf16(a[0], a[1]); w.y = cvt_pk_bf16(a[2], a[3]); w.z = cvt_pk_bf16(b[0], b[1]); w.w = cvt_pk_bf16(b[2], b[3]); return w; }
; __device__ __forceinline__ float silu_f(float x) { return x * __builtin_amdgcn_rcpf(1.0f + __builtin_amdgcn_exp2f(-1.4426950409f * x)); }
;     __device__ __forceinline__ void operator()(const f32x4 (&acc)[2][2][4][2], const Unit& u, int wr, int wc, int fr, int fq) const {
;     ...
;             PG8_LAS float* t = tab + wid * 128; rs_table<4, 16, 0>(part, u.pm * BM, wr, lane, 1.0f / DM, t);
; #pragma unroll
;             for (int ai = 0; ai < 2; ++ai)
; #pragma unroll
;                 for (int m = 0; m < 4; ++m) rs[ai][m] = t[ai * 64 + m * 16 + fr];
;         }
;         const int row0 = u.pm * BM + wr * 64 + fr, col0 = u.pn * HALF + wc * 32 + 8 * fq;
; #pragma unroll
;         for (int ai = 0; ai < 2; ++ai)
; #pragma unroll
;             for (int m = 0; m < 4; ++m) {
;                 const float r = rs[ai][m]; f32x4 o[2];
; #pragma unroll
;                 for (int n = 0; n < 2; ++n) { const f32x4 a = acc[ai][0][m][n] * r, b = acc[ai][1][m][n] * r;
;                     o[n] = (f32x4){silu_f(a[0]) * b[0], silu_f(a[1]) * b[1], silu_f(a[2]) * b[2], silu_f(a[3]) * b[3]}; }
;                 if (F8OUT) { u32x2 w; w.x = pack4_fp8(o[0]); w.y = pack4_fp8(o[1]); *(u32x2*)((unsigned char*)h + (size_t)(row0 + ai * HALF + m * 16) * FFN + col0) = w; }
;                 else *(u32x4*)(h + (size_t)(row0 + ai * HALF + m * 16) * FFN + col0) = pack8(o[0], o[1]);
	v_pk_mul_f32 v[26:27], v[18:19], v[26:27]
	v_pk_mul_f32 v[28:29], v[20:21], v[28:29]
	v_pk_mul_f32 v[30:31], v[22:23], v[30:31]
	v_pk_mul_f32 v[16:17], v[138:139], v[10:11] op_sel:[0,1]
	v_pk_mul_f32 v[18:19], v[140:141], v[10:11] op_sel:[0,1]
	v_pk_mul_f32 v[20:21], v[130:131], v[10:11] op_sel:[0,1]
	v_pk_mul_f32 v[22:23], v[132:133], v[10:11] op_sel:[0,1]
	v_pk_mul_f32 v[24:25], v[16:17], v[24:25]
	v_pk_mul_f32 v[26:27], v[18:19], v[26:27]
	v_pk_mul_f32 v[28:29], v[20:21], v[28:29]
	v_pk_mul_f32 v[30:31], v[22:23], v[30:31]
	v_pk_mul_f32 v[24:25], v[24:25], v[32:33] op_sel_hi:[1,0]
	v_pk_mul_f32 v[26:27], v[26:27], v[32:33] op_sel_hi:[1,0]
	v_pk_mul_f32 v[28:29], v[28:29], v[32:33] op_sel_hi:[1,0]
	v_pk_mul_f32 v[30:31], v[30:31], v[32:33] op_sel_hi:[1,0]
	v_med3_f32 v24, v24, s64, v250
	v_med3_f32 v25, v25, s64, v250
	v_med3_f32 v26, v26, s64, v250
	v_med3_f32 v27, v27, s64, v250
	v_med3_f32 v28, v28, s64, v250
	v_med3_f32 v29, v29, s64, v250
	v_med3_f32 v30, v30, s64, v250
	v_med3_f32 v31, v31, s64, v250
	v_cvt_pk_fp8_f32 v12, v24, v25
	v_cvt_pk_fp8_f32 v13, v28, v29
	s_nop 0
	v_cvt_pk_fp8_f32 v12, v26, v27 op_sel:[0,0,1]
	v_cvt_pk_fp8_f32 v13, v30, v31 op_sel:[0,0,1]
	v_or_b32_e32 v16, 16, v14
	v_mad_i64_i32 v[16:17], s[24:25], v16, s73, v[2:3]
	global_store_dwordx2 v[16:17], v[12:13], off
	v_pk_mul_f32 v[16:17], v[126:127], v[8:9] op_sel_hi:[1,0]
	v_pk_mul_f32 v[18:19], v[128:129], v[8:9] op_sel_hi:[1,0]
	v_pk_mul_f32 v[20:21], v[118:119], v[8:9] op_sel_hi:[1,0]
	v_pk_mul_f32 v[22:23], v[120:121], v[8:9] op_sel_hi:[1,0]
	v_pk_mul_f32 v[24:25], v[16:17], v[32:33] op_sel:[0,1]
	v_pk_mul_f32 v[26:27], v[18:19], v[32:33] op_sel:[0,1]
	v_pk_mul_f32 v[28:29], v[20:21], v[32:33] op_sel:[0,1]
	v_pk_mul_f32 v[30:31], v[22:23], v[32:33] op_sel:[0,1]
	v_exp_f32_e32 v24, v24
	v_exp_f32_e32 v25, v25
	v_exp_f32_e32 v26, v26
	v_exp_f32_e32 v27, v27
	v_exp_f32_e32 v28, v28
	v_exp_f32_e32 v29, v29
	v_exp_f32_e32 v30, v30
	v_exp_f32_e32 v31, v31
	v_pk_add_f32 v[24:25], v[24:25], v[14:15] op_sel:[0,1]
	v_pk_add_f32 v[26:27], v[26:27], v[14:15] op_sel:[0,1]
	v_pk_add_f32 v[28:29], v[28:29], v[14:15] op_sel:[0,1]
	v_pk_add_f32 v[30:31], v[30:31], v[14:15] op_sel:[0,1]
	v_rcp_f32_e32 v24, v24
	v_rcp_f32_e32 v25, v25
	v_rcp_f32_e32 v26, v26
	v_rcp_f32_e32 v27, v27
	v_rcp_f32_e32 v28, v28
	v_rcp_f32_e32 v29, v29
	v_rcp_f32_e32 v30, v30
	v_rcp_f32_e32 v31, v31
	v_pk_mul_f32 v[24:25], v[16:17], v[24:25]
	v_pk_mul_f32 v[26:27], v[18:19], v[26:27]
	v_pk_mul_f32 v[28:29], v[20:21], v[28:29]
	v_pk_mul_f32 v[30:31], v[22:23], v[30:31]
	v_pk_mul_f32 v[16:17], v[122:123], v[8:9] op_sel_hi:[1,0]
	v_pk_mul_f32 v[18:19], v[124:125], v[8:9] op_sel_hi:[1,0]
	v_pk_mul_f32 v[20:21], v[114:115], v[8:9] op_sel_hi:[1,0]
	v_pk_mul_f32 v[22:23], v[116:117], v[8:9] op_sel_hi:[1,0]
	v_pk_mul_f32 v[24:25], v[16:17], v[24:25]
	v_pk_mul_f32 v[26:27], v[18:19], v[26:27]
	v_pk_mul_f32 v[28:29], v[20:21], v[28:29]
	v_pk_mul_f32 v[30:31], v[22:23], v[30:31]
	v_pk_mul_f32 v[24:25], v[24:25], v[32:33] op_sel_hi:[1,0]
	v_pk_mul_f32 v[26:27], v[26:27], v[32:33] op_sel_hi:[1,0]
	v_pk_mul_f32 v[28:29], v[28:29], v[32:33] op_sel_hi:[1,0]
	v_pk_mul_f32 v[30:31], v[30:31], v[32:33] op_sel_hi:[1,0]
	v_med3_f32 v24, v24, s64, v250
	v_med3_f32 v25, v25, s64, v250
	v_med3_f32 v26, v26, s64, v250
	v_med3_f32 v27, v27, s64, v250
	v_med3_f32 v28, v28, s64, v250
	v_med3_f32 v29, v29, s64, v250
	v_med3_f32 v30, v30, s64, v250
	v_med3_f32 v31, v31, s64, v250
	v_cvt_pk_fp8_f32 v12, v24, v25
	v_cvt_pk_fp8_f32 v13, v28, v29
	s_nop 0
	v_cvt_pk_fp8_f32 v12, v26, v27 op_sel:[0,0,1]
	v_cvt_pk_fp8_f32 v13, v30, v31 op_sel:[0,0,1]
	v_or_b32_e32 v16, 32, v14
	v_mad_i64_i32 v[16:17], s[24:25], v16, s73, v[2:3]
	global_store_dwordx2 v[16:17], v[12:13], off
	v_pk_mul_f32 v[16:17], v[110:111], v[8:9] op_sel:[0,1]
	v_pk_mul_f32 v[18:19], v[112:113], v[8:9] op_sel:[0,1]
	v_pk_mul_f32 v[20:21], v[102:103], v[8:9] op_sel:[0,1]
	v_pk_mul_f32 v[22:23], v[104:105], v[8:9] op_sel:[0,1]
	v_pk_mul_f32 v[24:25], v[16:17], v[32:33] op_sel:[0,1]
	v_pk_mul_f32 v[26:27], v[18:19], v[32:33] op_sel:[0,1]
	v_pk_mul_f32 v[28:29], v[20:21], v[32:33] op_sel:[0,1]
	v_pk_mul_f32 v[30:31], v[22:23], v[32:33] op_sel:[0,1]
	v_exp_f32_e32 v24, v24
	v_exp_f32_e32 v25, v25
	v_exp_f32_e32 v26, v26
	v_exp_f32_e32 v27, v27
	v_exp_f32_e32 v28, v28
	v_exp_f32_e32 v29, v29
	v_exp_f32_e32 v30, v30
	v_exp_f32_e32 v31, v31
	v_pk_add_f32 v[24:25], v[24:25], v[14:15] op_sel:[0,1]
	v_pk_add_f32 v[26:27], v[26:27], v[14:15] op_sel:[0,1]
	v_pk_add_f32 v[28:29], v[28:29], v[14:15] op_sel:[0,1]
	v_pk_add_f32 v[30:31], v[30:31], v[14:15] op_sel:[0,1]
	v_rcp_f32_e32 v24, v24
	v_rcp_f32_e32 v25, v25
	v_rcp_f32_e32 v26, v26
	v_rcp_f32_e32 v27, v27
	v_rcp_f32_e32 v28, v28
	v_rcp_f32_e32 v29, v29
	v_rcp_f32_e32 v30, v30
	v_rcp_f32_e32 v31, v31
	v_pk_mul_f32 v[24:25], v[16:17], v[24:25]
	v_pk_mul_f32 v[26:27], v[18:19], v[26:27]
	v_pk_mul_f32 v[28:29], v[20:21], v[28:29]
	v_pk_mul_f32 v[30:31], v[22:23], v[30:31]
	v_pk_mul_f32 v[16:17], v[106:107], v[8:9] op_sel:[0,1]
	v_pk_mul_f32 v[18:19], v[108:109], v[8:9] op_sel:[0,1]
	v_pk_mul_f32 v[20:21], v[98:99], v[8:9] op_sel:[0,1]
	v_pk_mul_f32 v[22:23], v[100:101], v[8:9] op_sel:[0,1]
	v_pk_mul_f32 v[24:25], v[16:17], v[24:25]
	v_pk_mul_f32 v[26:27], v[18:19], v[26:27]
	v_pk_mul_f32 v[28:29], v[20:21], v[28:29]
	v_pk_mul_f32 v[30:31], v[22:23], v[30:31]
	v_pk_mul_f32 v[24:25], v[24:25], v[32:33] op_sel_hi:[1,0]
	v_pk_mul_f32 v[26:27], v[26:27], v[32:33] op_sel_hi:[1,0]
	v_pk_mul_f32 v[28:29], v[28:29], v[32:33] op_sel_hi:[1,0]
	v_pk_mul_f32 v[30:31], v[30:31], v[32:33] op_sel_hi:[1,0]
	v_med3_f32 v24, v24, s64, v250
; #define PG8_LAS __attribute__((address_space(3)))
; __device__ __forceinline__ u32x4 pack8(const f32x4 a, const f32x4 b) { u32x4 w; w.x = cvt_pk_bf16(a[0], a[1]); w.y = cvt_pk_bf16(a[2], a[3]); w.z = cvt_pk_bf16(b[0], b[1]); w.w = cvt_pk_bf16(b[2], b[3]); return w; }
; __device__ __forceinline__ float silu_f(float x) { return x * __builtin_amdgcn_rcpf(1.0f + __builtin_amdgcn_exp2f(-1.4426950409f * x)); }
;     __device__ __forceinline__ void operator()(const f32x4 (&acc)[2][2][4][2], const Unit& u, int wr, int wc, int fr, int fq) const {
;     ...
;             PG8_LAS float* t = tab + wid * 128; rs_table<4, 16, 0>(part, u.pm * BM, wr, lane, 1.0f / DM, t);
; #pragma unroll
;             for (int ai = 0; ai < 2; ++ai)
; #pragma unroll
;                 for (int m = 0; m < 4; ++m) rs[ai][m] = t[ai * 64 + m * 16 + fr];
;         }
;         const int row0 = u.pm * BM + wr * 64 + fr, col0 = u.pn * HALF + wc * 32 + 8 * fq;
; #pragma unroll
;         for (int ai = 0; ai < 2; ++ai)
; #pragma unroll
;             for (int m = 0; m < 4; ++m) {
;                 const float r = rs[ai][m]; f32x4 o[2];
; #pragma unroll
;                 for (int n = 0; n < 2; ++n) { const f32x4 a = acc[ai][0][m][n] * r, b = acc[ai][1][m][n] * r;
;                     o[n] = (f32x4){silu_f(a[0]) * b[0], silu_f(a[1]) * b[1], silu_f(a[2]) * b[2], silu_f(a[3]) * b[3]}; }
;                 if (F8OUT) { u32x2 w; w.x = pack4_fp8(o[0]); w.y = pack4_fp8(o[1]); *(u32x2*)((unsigned char*)h + (size_t)(row0 + ai * HALF + m * 16) * FFN + col0) = w; }
;                 else *(u32x4*)(h + (size_t)(row0 + ai * HALF + m * 16) * FFN + col0) = pack8(o[0], o[1]);
	v_med3_f32 v25, v25, s64, v250
	v_med3_f32 v26, v26, s64, v250
	v_med3_f32 v27, v27, s64, v250
	v_med3_f32 v28, v28, s64, v250
	v_med3_f32 v29, v29, s64, v250
	v_med3_f32 v30, v30, s64, v250
	v_med3_f32 v31, v31, s64, v250
	v_cvt_pk_fp8_f32 v12, v24, v25
	v_cvt_pk_fp8_f32 v13, v28, v29
	s_nop 0
	v_cvt_pk_fp8_f32 v12, v26, v27 op_sel:[0,0,1]
	v_cvt_pk_fp8_f32 v13, v30, v31 op_sel:[0,0,1]
	v_or_b32_e32 v16, 48, v14
	v_mad_i64_i32 v[16:17], s[24:25], v16, s73, v[2:3]
	global_store_dwordx2 v[16:17], v[12:13], off
	v_pk_mul_f32 v[16:17], v[94:95], v[6:7] op_sel_hi:[1,0]
	v_pk_mul_f32 v[18:19], v[96:97], v[6:7] op_sel_hi:[1,0]
	v_pk_mul_f32 v[20:21], v[86:87], v[6:7] op_sel_hi:[1,0]
	v_pk_mul_f32 v[22:23], v[88:89], v[6:7] op_sel_hi:[1,0]
	v_pk_mul_f32 v[24:25], v[16:17], v[32:33] op_sel:[0,1]
	v_pk_mul_f32 v[26:27], v[18:19], v[32:33] op_sel:[0,1]
	v_pk_mul_f32 v[28:29], v[20:21], v[32:33] op_sel:[0,1]
	v_pk_mul_f32 v[30:31], v[22:23], v[32:33] op_sel:[0,1]
	v_exp_f32_e32 v24, v24
	v_exp_f32_e32 v25, v25
	v_exp_f32_e32 v26, v26
	v_exp_f32_e32 v27, v27
	v_exp_f32_e32 v28, v28
	v_exp_f32_e32 v29, v29
	v_exp_f32_e32 v30, v30
	v_exp_f32_e32 v31, v31
	v_pk_add_f32 v[24:25], v[24:25], v[14:15] op_sel:[0,1]
	v_pk_add_f32 v[26:27], v[26:27], v[14:15] op_sel:[0,1]
	v_pk_add_f32 v[28:29], v[28:29], v[14:15] op_sel:[0,1]
	v_pk_add_f32 v[30:31], v[30:31], v[14:15] op_sel:[0,1]
	v_rcp_f32_e32 v24, v24
	v_rcp_f32_e32 v25, v25
	v_rcp_f32_e32 v26, v26
	v_rcp_f32_e32 v27, v27
	v_rcp_f32_e32 v28, v28
	v_rcp_f32_e32 v29, v29
	v_rcp_f32_e32 v30, v30
	v_rcp_f32_e32 v31, v31
	v_pk_mul_f32 v[24:25], v[16:17], v[24:25]
	v_pk_mul_f32 v[26:27], v[18:19], v[26:27]
	v_pk_mul_f32 v[28:29], v[20:21], v[28:29]
	v_pk_mul_f32 v[30:31], v[22:23], v[30:31]
	v_pk_mul_f32 v[16:17], v[90:91], v[6:7] op_sel_hi:[1,0]
	v_pk_mul_f32 v[18:19], v[92:93], v[6:7] op_sel_hi:[1,0]
	v_pk_mul_f32 v[20:21], v[82:83], v[6:7] op_sel_hi:[1,0]
	v_pk_mul_f32 v[22:23], v[84:85], v[6:7] op_sel_hi:[1,0]
	v_pk_mul_f32 v[24:25], v[16:17], v[24:25]
	v_pk_mul_f32 v[26:27], v[18:19], v[26:27]
	v_pk_mul_f32 v[28:29], v[20:21], v[28:29]
	v_pk_mul_f32 v[30:31], v[22:23], v[30:31]
	v_pk_mul_f32 v[24:25], v[24:25], v[32:33] op_sel_hi:[1,0]
	v_pk_mul_f32 v[26:27], v[26:27], v[32:33] op_sel_hi:[1,0]
	v_pk_mul_f32 v[28:29], v[28:29], v[32:33] op_sel_hi:[1,0]
	v_pk_mul_f32 v[30:31], v[30:31], v[32:33] op_sel_hi:[1,0]
	v_med3_f32 v24, v24, s64, v250
	v_med3_f32 v25, v25, s64, v250
	v_med3_f32 v26, v26, s64, v250
	v_med3_f32 v27, v27, s64, v250
	v_med3_f32 v28, v28, s64, v250
	v_med3_f32 v29, v29, s64, v250
	v_med3_f32 v30, v30, s64, v250
	v_med3_f32 v31, v31, s64, v250
	v_cvt_pk_fp8_f32 v12, v24, v25
	v_cvt_pk_fp8_f32 v13, v28, v29
	s_nop 0
	v_cvt_pk_fp8_f32 v12, v26, v27 op_sel:[0,0,1]
	v_cvt_pk_fp8_f32 v13, v30, v31 op_sel:[0,0,1]
	v_add_u32_e32 v16, 0x80, v14
	v_mad_i64_i32 v[16:17], s[24:25], v16, s73, v[2:3]
	global_store_dwordx2 v[16:17], v[12:13], off
	v_pk_mul_f32 v[16:17], v[78:79], v[6:7] op_sel:[0,1]
	v_pk_mul_f32 v[18:19], v[80:81], v[6:7] op_sel:[0,1]
	v_pk_mul_f32 v[20:21], v[70:71], v[6:7] op_sel:[0,1]
	v_pk_mul_f32 v[22:23], v[72:73], v[6:7] op_sel:[0,1]
	v_pk_mul_f32 v[24:25], v[16:17], v[32:33] op_sel:[0,1]
	v_pk_mul_f32 v[26:27], v[18:19], v[32:33] op_sel:[0,1]
	v_pk_mul_f32 v[28:29], v[20:21], v[32:33] op_sel:[0,1]
	v_pk_mul_f32 v[30:31], v[22:23], v[32:33] op_sel:[0,1]
	v_exp_f32_e32 v24, v24
	v_exp_f32_e32 v25, v25
	v_exp_f32_e32 v26, v26
	v_exp_f32_e32 v27, v27
	v_exp_f32_e32 v28, v28
	v_exp_f32_e32 v29, v29
	v_exp_f32_e32 v30, v30
	v_exp_f32_e32 v31, v31
	v_pk_add_f32 v[24:25], v[24:25], v[14:15] op_sel:[0,1]
	v_pk_add_f32 v[26:27], v[26:27], v[14:15] op_sel:[0,1]
	v_pk_add_f32 v[28:29], v[28:29], v[14:15] op_sel:[0,1]
	v_pk_add_f32 v[30:31], v[30:31], v[14:15] op_sel:[0,1]
	v_rcp_f32_e32 v24, v24
	v_rcp_f32_e32 v25, v25
	v_rcp_f32_e32 v26, v26
	v_rcp_f32_e32 v27, v27
	v_rcp_f32_e32 v28, v28
	v_rcp_f32_e32 v29, v29
	v_rcp_f32_e32 v30, v30
	v_rcp_f32_e32 v31, v31
	v_pk_mul_f32 v[24:25], v[16:17], v[24:25]
	v_pk_mul_f32 v[26:27], v[18:19], v[26:27]
	v_pk_mul_f32 v[28:29], v[20:21], v[28:29]
	v_pk_mul_f32 v[30:31], v[22:23], v[30:31]
	v_pk_mul_f32 v[16:17], v[74:75], v[6:7] op_sel:[0,1]
	v_pk_mul_f32 v[18:19], v[76:77], v[6:7] op_sel:[0,1]
	v_pk_mul_f32 v[20:21], v[66:67], v[6:7] op_sel:[0,1]
	v_pk_mul_f32 v[22:23], v[68:69], v[6:7] op_sel:[0,1]
	v_pk_mul_f32 v[24:25], v[16:17], v[24:25]
	v_pk_mul_f32 v[26:27], v[18:19], v[26:27]
	v_pk_mul_f32 v[28:29], v[20:21], v[28:29]
	v_pk_mul_f32 v[30:31], v[22:23], v[30:31]
	v_pk_mul_f32 v[24:25], v[24:25], v[32:33] op_sel_hi:[1,0]
	v_pk_mul_f32 v[26:27], v[26:27], v[32:33] op_sel_hi:[1,0]
	v_pk_mul_f32 v[28:29], v[28:29], v[32:33] op_sel_hi:[1,0]
	v_pk_mul_f32 v[30:31], v[30:31], v[32:33] op_sel_hi:[1,0]
	v_med3_f32 v24, v24, s64, v250
	v_med3_f32 v25, v25, s64, v250
	v_med3_f32 v26, v26, s64, v250
	v_med3_f32 v27, v27, s64, v250
	v_med3_f32 v28, v28, s64, v250
	v_med3_f32 v29, v29, s64, v250
	v_med3_f32 v30, v30, s64, v250
	v_med3_f32 v31, v31, s64, v250
	v_cvt_pk_fp8_f32 v12, v24, v25
	v_cvt_pk_fp8_f32 v13, v28, v29
	s_nop 0
	v_cvt_pk_fp8_f32 v12, v26, v27 op_sel:[0,0,1]
; #define PG8_LAS __attribute__((address_space(3)))
; __device__ __forceinline__ u32x4 pack8(const f32x4 a, const f32x4 b) { u32x4 w; w.x = cvt_pk_bf16(a[0], a[1]); w.y = cvt_pk_bf16(a[2], a[3]); w.z = cvt_pk_bf16(b[0], b[1]); w.w = cvt_pk_bf16(b[2], b[3]); return w; }
; __device__ __forceinline__ float silu_f(float x) { return x * __builtin_amdgcn_rcpf(1.0f + __builtin_amdgcn_exp2f(-1.4426950409f * x)); }
;     __device__ __forceinline__ void operator()(const f32x4 (&acc)[2][2][4][2], const Unit& u, int wr, int wc, int fr, int fq) const {
;     ...
;             PG8_LAS float* t = tab + wid * 128; rs_table<4, 16, 0>(part, u.pm * BM, wr, lane, 1.0f / DM, t);
; #pragma unroll
;             for (int ai = 0; ai < 2; ++ai)
; #pragma unroll
;                 for (int m = 0; m < 4; ++m) rs[ai][m] = t[ai * 64 + m * 16 + fr];
;         }
;         const int row0 = u.pm * BM + wr * 64 + fr, col0 = u.pn * HALF + wc * 32 + 8 * fq;
; #pragma unroll
;         for (int ai = 0; ai < 2; ++ai)
; #pragma unroll
;             for (int m = 0; m < 4; ++m) {
;                 const float r = rs[ai][m]; f32x4 o[2];
; #pragma unroll
;                 for (int n = 0; n < 2; ++n) { const f32x4 a = acc[ai][0][m][n] * r, b = acc[ai][1][m][n] * r;
;                     o[n] = (f32x4){silu_f(a[0]) * b[0], silu_f(a[1]) * b[1], silu_f(a[2]) * b[2], silu_f(a[3]) * b[3]}; }
;                 if (F8OUT) { u32x2 w; w.x = pack4_fp8(o[0]); w.y = pack4_fp8(o[1]); *(u32x2*)((unsigned char*)h + (size_t)(row0 + ai * HALF + m * 16) * FFN + col0) = w; }
;                 else *(u32x4*)(h + (size_t)(row0 + ai * HALF + m * 16) * FFN + col0) = pack8(o[0], o[1]);
	v_cvt_pk_fp8_f32 v13, v30, v31 op_sel:[0,0,1]
	v_add_u32_e32 v16, 0x90, v14
	v_mad_i64_i32 v[16:17], s[24:25], v16, s73, v[2:3]
	global_store_dwordx2 v[16:17], v[12:13], off
	v_pk_mul_f32 v[16:17], v[62:63], v[4:5] op_sel_hi:[1,0]
	v_pk_mul_f32 v[18:19], v[64:65], v[4:5] op_sel_hi:[1,0]
	v_pk_mul_f32 v[20:21], v[54:55], v[4:5] op_sel_hi:[1,0]
	v_pk_mul_f32 v[22:23], v[56:57], v[4:5] op_sel_hi:[1,0]
	v_pk_mul_f32 v[24:25], v[16:17], v[32:33] op_sel:[0,1]
	v_pk_mul_f32 v[26:27], v[18:19], v[32:33] op_sel:[0,1]
	v_pk_mul_f32 v[28:29], v[20:21], v[32:33] op_sel:[0,1]
	v_pk_mul_f32 v[30:31], v[22:23], v[32:33] op_sel:[0,1]
	v_exp_f32_e32 v24, v24
	v_exp_f32_e32 v25, v25
	v_exp_f32_e32 v26, v26
	v_exp_f32_e32 v27, v27
	v_exp_f32_e32 v28, v28
	v_exp_f32_e32 v29, v29
	v_exp_f32_e32 v30, v30
	v_exp_f32_e32 v31, v31
	v_pk_add_f32 v[24:25], v[24:25], v[14:15] op_sel:[0,1]
	v_pk_add_f32 v[26:27], v[26:27], v[14:15] op_sel:[0,1]
	v_pk_add_f32 v[28:29], v[28:29], v[14:15] op_sel:[0,1]
	v_pk_add_f32 v[30:31], v[30:31], v[14:15] op_sel:[0,1]
	v_rcp_f32_e32 v24, v24
	v_rcp_f32_e32 v25, v25
	v_rcp_f32_e32 v26, v26
	v_rcp_f32_e32 v27, v27
	v_rcp_f32_e32 v28, v28
	v_rcp_f32_e32 v29, v29
	v_rcp_f32_e32 v30, v30
	v_rcp_f32_e32 v31, v31
	v_pk_mul_f32 v[24:25], v[16:17], v[24:25]
	v_pk_mul_f32 v[26:27], v[18:19], v[26:27]
	v_pk_mul_f32 v[28:29], v[20:21], v[28:29]
	v_pk_mul_f32 v[30:31], v[22:23], v[30:31]
	v_pk_mul_f32 v[16:17], v[58:59], v[4:5] op_sel_hi:[1,0]
	v_pk_mul_f32 v[18:19], v[60:61], v[4:5] op_sel_hi:[1,0]
	v_pk_mul_f32 v[20:21], v[50:51], v[4:5] op_sel_hi:[1,0]
	v_pk_mul_f32 v[22:23], v[52:53], v[4:5] op_sel_hi:[1,0]
	v_pk_mul_f32 v[24:25], v[16:17], v[24:25]
	v_pk_mul_f32 v[26:27], v[18:19], v[26:27]
	v_pk_mul_f32 v[28:29], v[20:21], v[28:29]
	v_pk_mul_f32 v[30:31], v[22:23], v[30:31]
	v_pk_mul_f32 v[24:25], v[24:25], v[32:33] op_sel_hi:[1,0]
	v_pk_mul_f32 v[26:27], v[26:27], v[32:33] op_sel_hi:[1,0]
	v_pk_mul_f32 v[28:29], v[28:29], v[32:33] op_sel_hi:[1,0]
	v_pk_mul_f32 v[30:31], v[30:31], v[32:33] op_sel_hi:[1,0]
	v_med3_f32 v24, v24, s64, v250
	v_med3_f32 v25, v25, s64, v250
	v_med3_f32 v26, v26, s64, v250
	v_med3_f32 v27, v27, s64, v250
	v_med3_f32 v28, v28, s64, v250
	v_med3_f32 v29, v29, s64, v250
	v_med3_f32 v30, v30, s64, v250
	v_med3_f32 v31, v31, s64, v250
	v_cvt_pk_fp8_f32 v12, v24, v25
	v_cvt_pk_fp8_f32 v13, v28, v29
	s_nop 0
	v_cvt_pk_fp8_f32 v12, v26, v27 op_sel:[0,0,1]
	v_cvt_pk_fp8_f32 v13, v30, v31 op_sel:[0,0,1]
	v_add_u32_e32 v16, 0xa0, v14
	v_mad_i64_i32 v[16:17], s[24:25], v16, s73, v[2:3]
	global_store_dwordx2 v[16:17], v[12:13], off
	v_pk_mul_f32 v[16:17], v[46:47], v[4:5] op_sel:[0,1]
	v_pk_mul_f32 v[18:19], v[48:49], v[4:5] op_sel:[0,1]
	v_pk_mul_f32 v[20:21], v[38:39], v[4:5] op_sel:[0,1]
	v_pk_mul_f32 v[22:23], v[40:41], v[4:5] op_sel:[0,1]
	v_pk_mul_f32 v[24:25], v[16:17], v[32:33] op_sel:[0,1]
	v_pk_mul_f32 v[26:27], v[18:19], v[32:33] op_sel:[0,1]
	v_pk_mul_f32 v[28:29], v[20:21], v[32:33] op_sel:[0,1]
	v_pk_mul_f32 v[30:31], v[22:23], v[32:33] op_sel:[0,1]
	v_exp_f32_e32 v24, v24
	v_exp_f32_e32 v25, v25
	v_exp_f32_e32 v26, v26
	v_exp_f32_e32 v27, v27
	v_exp_f32_e32 v28, v28
	v_exp_f32_e32 v29, v29
	v_exp_f32_e32 v30, v30
	v_exp_f32_e32 v31, v31
	v_pk_add_f32 v[24:25], v[24:25], v[14:15] op_sel:[0,1]
	v_pk_add_f32 v[26:27], v[26:27], v[14:15] op_sel:[0,1]
	v_pk_add_f32 v[28:29], v[28:29], v[14:15] op_sel:[0,1]
	v_pk_add_f32 v[30:31], v[30:31], v[14:15] op_sel:[0,1]
	v_rcp_f32_e32 v24, v24
	v_rcp_f32_e32 v25, v25
	v_rcp_f32_e32 v26, v26
	v_rcp_f32_e32 v27, v27
	v_rcp_f32_e32 v28, v28
	v_rcp_f32_e32 v29, v29
	v_rcp_f32_e32 v30, v30
	v_rcp_f32_e32 v31, v31
	v_pk_mul_f32 v[24:25], v[16:17], v[24:25]
	v_pk_mul_f32 v[26:27], v[18:19], v[26:27]
	v_pk_mul_f32 v[28:29], v[20:21], v[28:29]
	v_pk_mul_f32 v[30:31], v[22:23], v[30:31]
	v_pk_mul_f32 v[16:17], v[42:43], v[4:5] op_sel:[0,1]
	v_pk_mul_f32 v[18:19], v[44:45], v[4:5] op_sel:[0,1]
	v_pk_mul_f32 v[20:21], v[34:35], v[4:5] op_sel:[0,1]
	v_pk_mul_f32 v[22:23], v[36:37], v[4:5] op_sel:[0,1]
	v_pk_mul_f32 v[24:25], v[16:17], v[24:25]
	v_pk_mul_f32 v[26:27], v[18:19], v[26:27]
	v_pk_mul_f32 v[28:29], v[20:21], v[28:29]
	v_pk_mul_f32 v[30:31], v[22:23], v[30:31]
	v_pk_mul_f32 v[24:25], v[24:25], v[32:33] op_sel_hi:[1,0]
	v_pk_mul_f32 v[26:27], v[26:27], v[32:33] op_sel_hi:[1,0]
	v_pk_mul_f32 v[28:29], v[28:29], v[32:33] op_sel_hi:[1,0]
	v_pk_mul_f32 v[30:31], v[30:31], v[32:33] op_sel_hi:[1,0]
	v_med3_f32 v24, v24, s64, v250
	v_med3_f32 v25, v25, s64, v250
	v_med3_f32 v26, v26, s64, v250
	v_med3_f32 v27, v27, s64, v250
	v_med3_f32 v28, v28, s64, v250
	v_med3_f32 v29, v29, s64, v250
	v_med3_f32 v30, v30, s64, v250
	v_med3_f32 v31, v31, s64, v250
	v_cvt_pk_fp8_f32 v12, v24, v25
	v_cvt_pk_fp8_f32 v13, v28, v29
	s_nop 0
	v_cvt_pk_fp8_f32 v12, v26, v27 op_sel:[0,0,1]
	v_cvt_pk_fp8_f32 v13, v30, v31 op_sel:[0,0,1]
	v_add_u32_e32 v16, 0xb0, v14
	v_mad_i64_i32 v[16:17], s[24:25], v16, s73, v[2:3]
	s_mov_b64 s[24:25], -1
	global_store_dwordx2 v[16:17], v[12:13], off
	s_cbranch_vccnz .LBB0_1719
	s_andn2_b64 vcc, exec, s[14:15]
	s_cbranch_vccnz .LBB0_1718
	s_barrier
	s_branch .LBB0_1718
